# final2 + chunk-attention loop: 16 provably dead zero-init v_mov before the bf8 pack removed
# baseline (speedup 1.0000x reference)
; #define ALAS __attribute__((address_space(3)))
; __device__ __forceinline__ bool chunk_unit_fast88(const Args& A, int b, int h, int qb, ALAS char* shm, const int tidb) {
;     ...
;             if (vis) {
;                 {
;                     ALAS const char* Ks_ = Kfr + ks1 * KSLOT;
;                     v8i kfa, kfb; C8_KFRAG(kfa, Ks_, 0); C8_KFRAG(kfb, Ks_, 1);
;                     mfma8_new(N0, kfa, qf, negm, sa8, sb8);
; #pragma unroll
;                     for (int e = 0; e < 16; ++e) C0[e] = __builtin_amdgcn_exp2f(C0[e]);
;                     __builtin_amdgcn_sched_barrier(0);
;                     mfma8_new(N1, kfb, qf, negm, sa8, sb8);
; #pragma unroll
;                     for (int e = 0; e < 16; ++e) C1[e] = __builtin_amdgcn_exp2f(C1[e]);
;                     __builtin_amdgcn_sched_barrier(0);
;                 }
;                 ALAS const char* vb_ = shm + L_V + vs * 4096 + lane * 16;
;                 v8i vf0, vf1;
;                 { const u32x4 a0 = *(ALAS const u32x4*)(vb_), a1 = *(ALAS const u32x4*)(vb_ + 1024), b0 = *(ALAS const u32x4*)(vb_ + 2048), b1 = *(ALAS const u32x4*)(vb_ + 3072);
;                   vf0 = (v8i){(int)a0.x, (int)a0.y, (int)a0.z, (int)a0.w, (int)a1.x, (int)a1.y, (int)a1.z, (int)a1.w}; vf1 = (v8i){(int)b0.x, (int)b0.y, (int)b0.z, (int)b0.w, (int)b1.x, (int)b1.y, (int)b1.z, (int)b1.w}; }
;                 v8i pf;
; #pragma unroll
;                 for (int kk = 0; kk < 4; ++kk) { const f32x16& cc_ = (kk < 2) ? C0 : C1; const int k8_ = 8 * (kk & 1);
;                     int w0_ = 0, w1_ = 0;
;                     w0_ = __builtin_amdgcn_cvt_pk_bf8_f32(cc_[k8_], cc_[k8_ + 1], w0_, false); w0_ = __builtin_amdgcn_cvt_pk_bf8_f32(cc_[k8_ + 2], cc_[k8_ + 3], w0_, true);
;                     w1_ = __builtin_amdgcn_cvt_pk_bf8_f32(cc_[k8_ + 4], cc_[k8_ + 5], w1_, false); w1_ = __builtin_amdgcn_cvt_pk_bf8_f32(cc_[k8_ + 6], cc_[k8_ + 7], w1_, true);
;                     pf[2 * kk] = w0_; pf[2 * kk + 1] = w1_; }
;                 __builtin_amdgcn_sched_barrier(0);
;                 mfma8p_acc(o0, pf, vf0, 0x7f7f7f7f, 0x7c7c7c7c);
;                 mfma8p_acc(o1, pf, vf1, 0x7f7f7f7f, 0x7c7c7c7c);
;                 mfma8p_acc(ls, pf, ones8, 0x7f7f7f7f, 0x7f7f7f7f);
;                 __builtin_amdgcn_sched_barrier(0);
.LBB0_799:
	s_andn2_b64 vcc, exec, s[52:53]
	s_cbranch_vccnz .LBB0_801
	v_lshl_add_u32 v0, s54, 12, v185
	v_exp_f32_e32 v64, v64
	v_exp_f32_e32 v65, v65
	v_exp_f32_e32 v66, v66
	v_exp_f32_e32 v67, v67
	v_exp_f32_e32 v68, v68
	v_exp_f32_e32 v69, v69
	v_exp_f32_e32 v70, v70
	v_exp_f32_e32 v71, v71
	v_exp_f32_e32 v72, v72
	v_exp_f32_e32 v73, v73
	v_exp_f32_e32 v74, v74
	v_exp_f32_e32 v75, v75
	v_exp_f32_e32 v76, v76
	v_exp_f32_e32 v77, v77
	v_exp_f32_e32 v78, v78
	v_exp_f32_e32 v79, v79
	ds_read_b128 v[2:5], v0
	ds_read_b128 v[6:9], v0 offset:1024
	ds_read_b128 v[224:227], v0 offset:2048
	ds_read_b128 v[228:231], v0 offset:3072
	s_waitcnt lgkmcnt(2)
	v_mfma_scale_f32_32x32x64_f8f6f4 v[112:127], v[2:9], v[144:151], v[48:63], v247, v253 op_sel_hi:[0,0,0]
	v_exp_f32_e32 v96, v96
	v_exp_f32_e32 v97, v97
	v_exp_f32_e32 v98, v98
	v_exp_f32_e32 v99, v99
	v_exp_f32_e32 v100, v100
	v_exp_f32_e32 v101, v101
	v_exp_f32_e32 v102, v102
	v_exp_f32_e32 v103, v103
	v_exp_f32_e32 v104, v104
	v_exp_f32_e32 v105, v105
	v_exp_f32_e32 v106, v106
	v_exp_f32_e32 v107, v107
	v_exp_f32_e32 v108, v108
	v_exp_f32_e32 v109, v109
	v_exp_f32_e32 v110, v110
	v_exp_f32_e32 v111, v111
	s_waitcnt lgkmcnt(0)
	v_mfma_scale_f32_32x32x64_f8f6f4 v[128:143], v[224:231], v[144:151], v[48:63], v247, v253 op_sel_hi:[0,0,0]
	ds_read_b128 v[2:5], v185 offset:36864
	ds_read_b128 v[6:9], v185 offset:37888
	ds_read_b128 v[224:227], v185 offset:38912
	ds_read_b128 v[228:231], v185 offset:39936
	v_cvt_pk_bf8_f32 v232, v64, v65
	v_cvt_pk_bf8_f32 v233, v68, v69
	v_cvt_pk_bf8_f32 v234, v72, v73
	v_cvt_pk_bf8_f32 v235, v76, v77
	v_cvt_pk_bf8_f32 v236, v96, v97
	v_cvt_pk_bf8_f32 v237, v100, v101
	v_cvt_pk_bf8_f32 v238, v104, v105
	v_cvt_pk_bf8_f32 v239, v108, v109
	v_cvt_pk_bf8_f32 v232, v66, v67 op_sel:[0,0,1]
	v_cvt_pk_bf8_f32 v233, v70, v71 op_sel:[0,0,1]
	v_cvt_pk_bf8_f32 v234, v74, v75 op_sel:[0,0,1]
	v_cvt_pk_bf8_f32 v235, v78, v79 op_sel:[0,0,1]
	v_cvt_pk_bf8_f32 v236, v98, v99 op_sel:[0,0,1]
	v_cvt_pk_bf8_f32 v237, v102, v103 op_sel:[0,0,1]
	v_cvt_pk_bf8_f32 v238, v106, v107 op_sel:[0,0,1]
	v_cvt_pk_bf8_f32 v239, v110, v111 op_sel:[0,0,1]
	s_waitcnt lgkmcnt(2)
	v_mfma_scale_f32_32x32x64_f8f6f4 v[32:47], v[232:239], v[2:9], v[32:47], v251, v247 op_sel_hi:[0,0,0] cbsz:1
	s_waitcnt lgkmcnt(0)
	v_mfma_scale_f32_32x32x64_f8f6f4 v[16:31], v[232:239], v[224:231], v[16:31], v251, v247 op_sel_hi:[0,0,0] cbsz:1
	v_mov_b32_e32 v163, v162
	v_mov_b32_e32 v164, v162
	v_mov_b32_e32 v165, v162
	v_mov_b32_e32 v166, v162
	v_mov_b32_e32 v167, v162
	v_mov_b32_e32 v168, v162
	v_mov_b32_e32 v169, v162
	v_mfma_scale_f32_32x32x64_f8f6f4 v[80:95], v[232:239], v[162:169], v[80:95], v251, v251 op_sel_hi:[0,0,0] cbsz:1

; #define ALAS __attribute__((address_space(3)))
; __device__ __forceinline__ bool chunk_unit_fast88(const Args& A, int b, int h, int qb, ALAS char* shm, const int tidb) {
;     ...
;             if (vis) {
;                 {
;                     ALAS const char* Ks_ = Kfr + ks1 * KSLOT;
;                     v8i kfa, kfb; C8_KFRAG(kfa, Ks_, 0); C8_KFRAG(kfb, Ks_, 1);
;                     mfma8_new(N0, kfa, qf, negm, sa8, sb8);
; #pragma unroll
;                     for (int e = 0; e < 16; ++e) C0[e] = __builtin_amdgcn_exp2f(C0[e]);
;                     __builtin_amdgcn_sched_barrier(0);
;                     mfma8_new(N1, kfb, qf, negm, sa8, sb8);
; #pragma unroll
;                     for (int e = 0; e < 16; ++e) C1[e] = __builtin_amdgcn_exp2f(C1[e]);
;                     __builtin_amdgcn_sched_barrier(0);
;                 }
;                 ALAS const char* vb_ = shm + L_V + vs * 4096 + lane * 16;
;                 v8i vf0, vf1;
;                 { const u32x4 a0 = *(ALAS const u32x4*)(vb_), a1 = *(ALAS const u32x4*)(vb_ + 1024), b0 = *(ALAS const u32x4*)(vb_ + 2048), b1 = *(ALAS const u32x4*)(vb_ + 3072);
;                   vf0 = (v8i){(int)a0.x, (int)a0.y, (int)a0.z, (int)a0.w, (int)a1.x, (int)a1.y, (int)a1.z, (int)a1.w}; vf1 = (v8i){(int)b0.x, (int)b0.y, (int)b0.z, (int)b0.w, (int)b1.x, (int)b1.y, (int)b1.z, (int)b1.w}; }
;                 v8i pf;
; #pragma unroll
;                 for (int kk = 0; kk < 4; ++kk) { const f32x16& cc_ = (kk < 2) ? C0 : C1; const int k8_ = 8 * (kk & 1);
;                     int w0_ = 0, w1_ = 0;
;                     w0_ = __builtin_amdgcn_cvt_pk_bf8_f32(cc_[k8_], cc_[k8_ + 1], w0_, false); w0_ = __builtin_amdgcn_cvt_pk_bf8_f32(cc_[k8_ + 2], cc_[k8_ + 3], w0_, true);
;                     w1_ = __builtin_amdgcn_cvt_pk_bf8_f32(cc_[k8_ + 4], cc_[k8_ + 5], w1_, false); w1_ = __builtin_amdgcn_cvt_pk_bf8_f32(cc_[k8_ + 6], cc_[k8_ + 7], w1_, true);
;                     pf[2 * kk] = w0_; pf[2 * kk + 1] = w1_; }
;                 __builtin_amdgcn_sched_barrier(0);
;                 mfma8p_acc(o0, pf, vf0, 0x7f7f7f7f, 0x7c7c7c7c);
;                 mfma8p_acc(o1, pf, vf1, 0x7f7f7f7f, 0x7c7c7c7c);
;                 mfma8p_acc(ls, pf, ones8, 0x7f7f7f7f, 0x7f7f7f7f);
;                 __builtin_amdgcn_sched_barrier(0);
.LBB0_811:
	s_andn2_b64 vcc, exec, s[34:35]
	s_cbranch_vccnz .LBB0_788
	v_lshl_add_u32 v0, s67, 12, v185
	v_exp_f32_e32 v112, v112
	v_exp_f32_e32 v113, v113
	v_exp_f32_e32 v114, v114
	v_exp_f32_e32 v115, v115
	v_exp_f32_e32 v116, v116
	v_exp_f32_e32 v117, v117
	v_exp_f32_e32 v118, v118
	v_exp_f32_e32 v119, v119
	v_exp_f32_e32 v120, v120
	v_exp_f32_e32 v121, v121
	v_exp_f32_e32 v122, v122
	v_exp_f32_e32 v123, v123
	v_exp_f32_e32 v124, v124
	v_exp_f32_e32 v125, v125
	v_exp_f32_e32 v126, v126
	v_exp_f32_e32 v127, v127
	ds_read_b128 v[2:5], v0
	ds_read_b128 v[6:9], v0 offset:1024
	ds_read_b128 v[224:227], v0 offset:2048
	ds_read_b128 v[228:231], v0 offset:3072
	s_waitcnt lgkmcnt(2)
	v_mfma_scale_f32_32x32x64_f8f6f4 v[64:79], v[2:9], v[144:151], v[48:63], v247, v253 op_sel_hi:[0,0,0]
	v_exp_f32_e32 v128, v128
	v_exp_f32_e32 v129, v129
	v_exp_f32_e32 v130, v130
	v_exp_f32_e32 v131, v131
	v_exp_f32_e32 v132, v132
	v_exp_f32_e32 v133, v133
	v_exp_f32_e32 v134, v134
	v_exp_f32_e32 v135, v135
	v_exp_f32_e32 v136, v136
	v_exp_f32_e32 v137, v137
	v_exp_f32_e32 v138, v138
	v_exp_f32_e32 v139, v139
	v_exp_f32_e32 v140, v140
	v_exp_f32_e32 v141, v141
	v_exp_f32_e32 v142, v142
	v_exp_f32_e32 v143, v143
	s_waitcnt lgkmcnt(0)
	v_mfma_scale_f32_32x32x64_f8f6f4 v[96:111], v[224:231], v[144:151], v[48:63], v247, v253 op_sel_hi:[0,0,0]
	ds_read_b128 v[2:5], v185 offset:40960
	ds_read_b128 v[6:9], v185 offset:41984
	ds_read_b128 v[224:227], v185 offset:43008
	ds_read_b128 v[228:231], v185 offset:44032
	v_cvt_pk_bf8_f32 v232, v112, v113
	v_cvt_pk_bf8_f32 v233, v116, v117
	v_cvt_pk_bf8_f32 v234, v120, v121
	v_cvt_pk_bf8_f32 v235, v124, v125
	v_cvt_pk_bf8_f32 v236, v128, v129
	v_cvt_pk_bf8_f32 v237, v132, v133
	v_cvt_pk_bf8_f32 v238, v136, v137
	v_cvt_pk_bf8_f32 v239, v140, v141
	v_cvt_pk_bf8_f32 v232, v114, v115 op_sel:[0,0,1]
	v_cvt_pk_bf8_f32 v233, v118, v119 op_sel:[0,0,1]
	v_cvt_pk_bf8_f32 v234, v122, v123 op_sel:[0,0,1]
	v_cvt_pk_bf8_f32 v235, v126, v127 op_sel:[0,0,1]
	v_cvt_pk_bf8_f32 v236, v130, v131 op_sel:[0,0,1]
	v_cvt_pk_bf8_f32 v237, v134, v135 op_sel:[0,0,1]
	v_cvt_pk_bf8_f32 v238, v138, v139 op_sel:[0,0,1]
	v_cvt_pk_bf8_f32 v239, v142, v143 op_sel:[0,0,1]
	s_waitcnt lgkmcnt(2)
	v_mfma_scale_f32_32x32x64_f8f6f4 v[32:47], v[232:239], v[2:9], v[32:47], v251, v247 op_sel_hi:[0,0,0] cbsz:1
	s_waitcnt lgkmcnt(0)
	v_mfma_scale_f32_32x32x64_f8f6f4 v[16:31], v[232:239], v[224:231], v[16:31], v251, v247 op_sel_hi:[0,0,0] cbsz:1
	v_mov_b32_e32 v163, v162
	v_mov_b32_e32 v164, v162
	v_mov_b32_e32 v165, v162
	v_mov_b32_e32 v166, v162
	v_mov_b32_e32 v167, v162
	v_mov_b32_e32 v168, v162
	v_mov_b32_e32 v169, v162
	v_mfma_scale_f32_32x32x64_f8f6f4 v[80:95], v[232:239], v[162:169], v[80:95], v251, v251 op_sel_hi:[0,0,0] cbsz:1
	s_branch .LBB0_788
